# baseline (speedup 1.0000x reference)
.LBB0_97:
	s_or_b64 exec, exec, s[40:41]
	global_load_dword v98, v108, s[58:59]
	global_load_dwordx4 v[74:77], v2, s[92:93]
	global_load_dwordx4 v[94:97], v2, s[92:93] offset:64
	global_load_dwordx4 v[120:123], v2, s[92:93] offset:128
	global_load_dwordx4 v[124:127], v2, s[92:93] offset:192
	s_cmp_lt_i32 s80, 0
	s_cbranch_scc1 .Lattn_skip
	v_mfma_f32_16x16x32_f16 v[104:107], v[66:69], v[6:9], 0
	v_or_b32_e32 v2, s94, v79
	v_cmp_lt_i32_e64 s[42:43], v2, s82
	v_cmp_ge_i32_e64 s[40:41], v2, s82
	v_mfma_f32_16x16x32_f16 v[104:107], v[62:65], v[10:13], v[104:107]
	s_and_b64 s[42:43], s[84:85], s[42:43]
	v_cndmask_b32_e64 v2, 0, 1, s[42:43]
	s_and_b64 s[40:41], s[40:41], s[84:85]
	v_cmp_ne_u32_e64 s[42:43], 0, v2
	v_cndmask_b32_e64 v2, 0, 1, s[40:41]
	v_mfma_f32_16x16x32_f16 v[104:107], v[58:61], v[14:17], v[104:107]
	v_cmp_ne_u32_e32 vcc, 0, v2
	v_mov_b32_e32 v5, s42
	v_cmp_ngt_f32_e64 s[48:49], s70, v103
	v_mov_b32_e32 v2, vcc_lo
	v_cndmask_b32_e64 v2, v2, v5, s[38:39]
	v_mfma_f32_16x16x32_f16 v[108:111], v[54:57], v[18:21], v[104:107]
	ds_write2_b64 v92, v[66:67], v[68:69] offset1:4
	ds_write2_b64 v92, v[62:63], v[64:65] offset0:8 offset1:12
	ds_read_b64_tr_b16 v[62:63], v93
	ds_read_b64_tr_b16 v[64:65], v93 offset:32
	ds_read_b64_tr_b16 v[68:69], v93 offset:64
	ds_read_b64_tr_b16 v[84:85], v93 offset:96
	ds_write2_b64 v92, v[58:59], v[60:61] offset1:4
	ds_write2_b64 v92, v[54:55], v[56:57] offset0:8 offset1:12
	ds_read_b64_tr_b16 v[54:55], v93
	ds_read_b64_tr_b16 v[56:57], v93 offset:32
	ds_read_b64_tr_b16 v[58:59], v93 offset:64
	ds_read_b64_tr_b16 v[60:61], v93 offset:96
	v_lshrrev_b32_sdwa v2, v88, v2 dst_sel:DWORD dst_unused:UNUSED_PAD src0_sel:DWORD src1_sel:WORD_0
	v_and_b32_e32 v5, 1, v2
	v_cmp_eq_u32_e64 s[46:47], 0, v5
	v_and_b32_e32 v5, 2, v2
	v_cmp_eq_u32_e64 s[40:41], 0, v5
	v_and_b32_e32 v104, 4, v2
	v_and_b32_e32 v2, 8, v2
	s_nop 0
	v_cndmask_b32_e64 v107, v108, v71, s[46:47]
	v_cndmask_b32_e64 v105, v109, v71, s[40:41]
	v_cmp_eq_u32_e64 s[42:43], 0, v104
	v_cmp_eq_u32_e64 s[44:45], 0, v2
	v_max3_f32 v5, v107, s69, v105
	v_cndmask_b32_e64 v106, v110, v71, s[42:43]
	v_cndmask_b32_e64 v104, v111, v71, s[44:45]
	v_max3_f32 v2, v5, v106, v104
	v_mov_b32_e32 v5, v2
	s_nop 1
	v_permlane16_swap_b32_e32 v5, v2
	v_max_f32_e32 v2, v2, v5
	v_mov_b32_e32 v5, v2
	s_nop 1
	v_permlane32_swap_b32_e32 v5, v2
	v_max_f32_e32 v108, v2, v5
	v_sub_f32_e32 v2, v108, v103
	v_cmp_lt_f32_e32 vcc, s71, v2
	s_and_b64 vcc, s[48:49], vcc
	s_nop 0
	v_cndmask_b32_e64 v2, 0, 1, vcc
	v_cmp_ne_u32_e64 s[50:51], 0, v2
	s_cmp_lg_u64 s[50:51], 0
	s_cselect_b64 s[50:51], -1, 0
	s_cbranch_vccz .LBB0_117
	v_max_f32_e32 v2, v108, v108
	v_max_f32_e32 v5, v103, v103
	v_max_f32_e32 v5, v5, v2
	v_sub_f32_e32 v2, v103, v5
	v_exp_f32_e32 v2, v2
	s_cbranch_execnz .LBB0_100

.LBB0_102:
	v_sub_f32_e32 v105, v105, v5
	v_sub_f32_e32 v104, v104, v5
	v_exp_f32_e32 v105, v105
	v_exp_f32_e32 v104, v104
	v_sub_f32_e32 v103, v107, v5
	v_cndmask_b32_e64 v107, v105, 0, s[40:41]
	v_cndmask_b32_e64 v108, v104, 0, s[44:45]
	v_sub_f32_e32 v106, v106, v5
	v_exp_f32_e32 v103, v103
	v_exp_f32_e32 v106, v106
	s_nop 0
	v_cndmask_b32_e64 v103, v103, 0, s[46:47]
	v_cndmask_b32_e64 v106, v106, 0, s[42:43]
	v_cvt_pk_f16_f32 v67, v106, v108
	v_cvt_pk_f16_f32 v66, v103, v107
	s_waitcnt lgkmcnt(3)
	s_cmp_eq_u32 s81, 0
	s_cbranch_scc1 .Lattn_g_first
	v_mfma_f32_16x16x16_f16 v[30:33], v[54:55], v[66:67], v[30:33]
	v_add_f32_e32 v54, 0, v103
	v_add_f32_e32 v54, v107, v54
	v_add_f32_e32 v54, v106, v54
	v_mfma_f32_16x16x16_f16 v[46:49], v[62:63], v[66:67], v[46:49]
	v_add_f32_e32 v54, v108, v54
	v_fmac_f32_e32 v54, v4, v2
	v_mfma_f32_16x16x16_f16 v[50:53], v[64:65], v[66:67], v[50:53]
	v_mfma_f32_16x16x16_f16 v[38:41], v[68:69], v[66:67], v[38:41]
	v_mfma_f32_16x16x16_f16 v[42:45], v[84:85], v[66:67], v[42:45]
	s_waitcnt lgkmcnt(2)
	v_mfma_f32_16x16x16_f16 v[34:37], v[56:57], v[66:67], v[34:37]
	s_waitcnt lgkmcnt(1)
	v_mfma_f32_16x16x16_f16 v[22:25], v[58:59], v[66:67], v[22:25]
	s_waitcnt lgkmcnt(0)
	v_mfma_f32_16x16x16_f16 v[26:29], v[60:61], v[66:67], v[26:29]
	s_branch .Lattn_g_done
.Lattn_g_first:
	v_mfma_f32_16x16x16_f16 v[30:33], v[54:55], v[66:67], 0
	v_add_f32_e32 v54, 0, v103
	v_add_f32_e32 v54, v107, v54
	v_add_f32_e32 v54, v106, v54
	v_mfma_f32_16x16x16_f16 v[46:49], v[62:63], v[66:67], 0
	v_add_f32_e32 v54, v108, v54
	v_fmac_f32_e32 v54, v4, v2
	v_mfma_f32_16x16x16_f16 v[50:53], v[64:65], v[66:67], 0
	v_mfma_f32_16x16x16_f16 v[38:41], v[68:69], v[66:67], 0
	v_mfma_f32_16x16x16_f16 v[42:45], v[84:85], v[66:67], 0
	s_waitcnt lgkmcnt(2)
	v_mfma_f32_16x16x16_f16 v[34:37], v[56:57], v[66:67], 0
	s_waitcnt lgkmcnt(1)
	v_mfma_f32_16x16x16_f16 v[22:25], v[58:59], v[66:67], 0
	s_waitcnt lgkmcnt(0)
	v_mfma_f32_16x16x16_f16 v[26:29], v[60:61], v[66:67], 0
